# s22 + P7 stagger: half of each XCD's workgroups start P7 about 12 us late so that their bandwidth-bound LN parts overlap the others' latency-bound router / top-4 parts
# speedup vs baseline: 1.0021x; 1.0019x over previous
; #define LAS __attribute__((address_space(3)))
; __global__ void __launch_bounds__(NTHREADS, 2) fwd(Args args) {
;     ...
;     if (IN(7)) {
;         LAS float* part = (LAS float*)lds;
;         LAS float* lgt = (LAS float*)(lds + 32768);
;         LAS int* selE = (LAS int*)(lds + 36864);
;         LAS unsigned* lcnt = (LAS unsigned*)(lds + 36864 + 512);
;         LAS unsigned* gbs = lcnt + 32;
;         if (tid < 32) lcnt[tid] = 0u;
.LBB0_752:
	s_cmp_lt_i32 s90, 8
	s_cselect_b64 s[2:3], -1, 0
	s_add_u32 s22, s88, 0x5b600000
	s_addc_u32 s23, s89, 0
	s_add_u32 s20, s88, 0x63600000
	s_addc_u32 s21, s89, 0
	s_add_u32 s24, s88, 0x63800000
	s_addc_u32 s25, s89, 0
	s_add_u32 s26, s88, 0x89a00000
	s_addc_u32 s27, s89, 0
	s_add_u32 s28, s88, 0x1000
	s_addc_u32 s29, s89, 0
	s_and_b64 s[0:1], s[2:3], s[0:1]
	s_andn2_b64 vcc, exec, s[0:1]
	v_cmp_gt_u32_e64 s[4:5], 32, v0
	s_cbranch_vccnz .LBB0_792
	s_bitcmp1_b32 s94, 3
	s_cbranch_scc0 .Lmy_p7_nodelay
	s_sleep 127
	s_sleep 127
	s_sleep 127
.Lmy_p7_nodelay:
	s_and_saveexec_b64 s[6:7], s[4:5]
	s_cbranch_execz .LBB0_755
	s_waitcnt vmcnt(0)
	v_mov_b32_e32 v2, 0
	ds_write_b32 v1, v2 offset:37376
